# same as v16 but the h1 barrier sits after the complete second own k-step
# speedup vs baseline: 1.0103x; 1.0000x over previous
.LBB1_4:
	s_and_saveexec_b64 s[8:9], s[2:3]
	v_perm_b32 v5, v1, v102, s23
	v_perm_b32 v9, v121, v103, s23
	v_perm_b32 v17, v144, v115, s23
	v_perm_b32 v29, v145, v116, s23
	s_or_b64 exec, exec, s[8:9]
	v_mfma_f32_16x16x32_f16 v[164:167], v[30:33], v[2:5], 0
	v_mfma_f32_16x16x32_f16 v[180:183], v[22:25], v[2:5], 0
	s_cmp_lg_u32 s22, 0x818000
	v_mfma_f32_16x16x32_f16 v[168:171], v[30:33], v[6:9], 0
	v_mfma_f32_16x16x32_f16 v[184:187], v[22:25], v[6:9], 0
	s_cselect_b32 s9, s11, 15
	v_mfma_f32_16x16x32_f16 v[172:175], v[30:33], v[14:17], 0
	v_mfma_f32_16x16x32_f16 v[188:191], v[22:25], v[14:17], 0
	v_mfma_f32_16x16x32_f16 v[176:179], v[30:33], v[26:29], 0
	v_mfma_f32_16x16x32_f16 v[192:195], v[22:25], v[26:29], 0
	v_mfma_f32_16x16x32_f16 v[208:211], v[18:21], v[2:5], 0
	v_cvt_pk_f16_f32 v122, v164, v165
	v_cvt_pk_f16_f32 v123, v166, v167
	v_pk_max_f16 v122, v122, 0
	v_pk_max_f16 v123, v123, 0
	v_cvt_pk_f16_f32 v124, v180, v181
	v_cvt_pk_f16_f32 v125, v182, v183
	v_pk_max_f16 v124, v124, 0
	v_pk_max_f16 v125, v125, 0
	ds_write_b128 v107, v[122:125]
	v_mfma_f32_16x16x32_f16 v[224:227], v[10:13], v[2:5], 0
	v_cvt_pk_f16_f32 v126, v168, v169
	v_cvt_pk_f16_f32 v127, v170, v171
	v_pk_max_f16 v126, v126, 0
	v_pk_max_f16 v127, v127, 0
	v_cvt_pk_f16_f32 v128, v184, v185
	v_cvt_pk_f16_f32 v129, v186, v187
	v_pk_max_f16 v128, v128, 0
	v_pk_max_f16 v129, v129, 0
	ds_write_b128 v107, v[126:129] offset:16384
	v_mfma_f32_16x16x32_f16 v[212:215], v[18:21], v[6:9], 0
	v_cvt_pk_f16_f32 v134, v172, v173
	v_cvt_pk_f16_f32 v135, v174, v175
	v_pk_max_f16 v134, v134, 0
	v_pk_max_f16 v135, v135, 0
	v_cvt_pk_f16_f32 v136, v188, v189
	v_cvt_pk_f16_f32 v137, v190, v191
	v_pk_max_f16 v136, v136, 0
	v_pk_max_f16 v137, v137, 0
	ds_write_b128 v107, v[134:137] offset:32768
	v_mfma_f32_16x16x32_f16 v[228:231], v[10:13], v[6:9], 0
	v_cvt_pk_f16_f32 v138, v176, v177
	v_cvt_pk_f16_f32 v139, v178, v179
	v_pk_max_f16 v138, v138, 0
	v_pk_max_f16 v139, v139, 0
	v_cvt_pk_f16_f32 v140, v192, v193
	v_cvt_pk_f16_f32 v141, v194, v195
	v_pk_max_f16 v140, v140, 0
	v_pk_max_f16 v141, v141, 0
	ds_write_b128 v107, v[138:141] offset:49152
	v_mfma_f32_16x16x32_f16 v[216:219], v[18:21], v[14:17], 0
	v_mfma_f32_16x16x32_f16 v[232:235], v[10:13], v[14:17], 0
	v_mfma_f32_16x16x32_f16 v[220:223], v[18:21], v[26:29], 0
	v_mfma_f32_16x16x32_f16 v[236:239], v[10:13], v[26:29], 0
	v_add_u32_e32 v111, s64, v111
	v_add_u32_e32 v98, s65, v98
	s_lshl_b32 s20, s9, 7
	v_lshl_add_u64 v[0:1], s[20:21], 3, v[132:133]
	s_add_i32 s25, s22, s34
	s_lshl_b32 s8, s9, 8
	buffer_load_dwordx4 v[192:195], v147, s[16:19], s25 offen
	buffer_load_dwordx4 v[196:199], v148, s[16:19], s25 offen
	buffer_load_dwordx4 v[200:203], v149, s[16:19], s25 offen
	buffer_load_dwordx4 v[204:207], v150, s[16:19], s25 offen
	s_waitcnt vmcnt(19)
	v_mfma_f32_16x16x32_f16 v[164:167], v[58:61], v[122:125], v[240:243]
	v_cvt_pk_f16_f32 v142, v208, v209
	v_cvt_pk_f16_f32 v143, v210, v211
	v_mfma_f32_16x16x32_f16 v[168:171], v[58:61], v[126:129], v[240:243]
	v_pk_max_f16 v142, v142, 0
	v_pk_max_f16 v143, v143, 0
	v_mfma_f32_16x16x32_f16 v[172:175], v[58:61], v[134:137], v[240:243]
	v_cvt_pk_f16_f32 v144, v224, v225
	v_cvt_pk_f16_f32 v145, v226, v227
	v_mfma_f32_16x16x32_f16 v[10:13], v[58:61], v[138:141], v[240:243]
	v_pk_max_f16 v144, v144, 0
	v_pk_max_f16 v145, v145, 0
	ds_write_b128 v108, v[142:145]
	s_waitcnt vmcnt(18)
	v_mfma_f32_16x16x32_f16 v[58:61], v[54:57], v[122:125], v[244:247]
	v_cvt_pk_f16_f32 v152, v212, v213
	v_cvt_pk_f16_f32 v153, v214, v215
	v_mfma_f32_16x16x32_f16 v[176:179], v[54:57], v[126:129], v[244:247]
	v_pk_max_f16 v152, v152, 0
	v_pk_max_f16 v153, v153, 0
	v_mfma_f32_16x16x32_f16 v[180:183], v[54:57], v[134:137], v[244:247]
	v_cvt_pk_f16_f32 v154, v228, v229
	v_cvt_pk_f16_f32 v155, v230, v231
	v_mfma_f32_16x16x32_f16 v[18:21], v[54:57], v[138:141], v[244:247]
	v_pk_max_f16 v154, v154, 0
	v_pk_max_f16 v155, v155, 0
	ds_write_b128 v108, v[152:155] offset:16384
	s_waitcnt vmcnt(17)
	v_mfma_f32_16x16x32_f16 v[54:57], v[50:53], v[122:125], v[248:251]
	v_cvt_pk_f16_f32 v156, v216, v217
	v_cvt_pk_f16_f32 v157, v218, v219
	v_mfma_f32_16x16x32_f16 v[184:187], v[50:53], v[126:129], v[248:251]
	v_pk_max_f16 v156, v156, 0
	v_pk_max_f16 v157, v157, 0
	v_mfma_f32_16x16x32_f16 v[188:191], v[50:53], v[134:137], v[248:251]
	v_cvt_pk_f16_f32 v158, v232, v233
	v_cvt_pk_f16_f32 v159, v234, v235
	v_mfma_f32_16x16x32_f16 v[22:25], v[50:53], v[138:141], v[248:251]
	v_pk_max_f16 v158, v158, 0
	v_pk_max_f16 v159, v159, 0
	ds_write_b128 v108, v[156:159] offset:32768
	s_waitcnt vmcnt(16)
	v_mfma_f32_16x16x32_f16 v[50:53], v[38:41], v[122:125], v[252:255]
	v_cvt_pk_f16_f32 v160, v220, v221
	v_cvt_pk_f16_f32 v161, v222, v223
	v_mfma_f32_16x16x32_f16 v[122:125], v[38:41], v[126:129], v[252:255]
	v_pk_max_f16 v160, v160, 0
	v_pk_max_f16 v161, v161, 0
	v_mfma_f32_16x16x32_f16 v[126:129], v[38:41], v[134:137], v[252:255]
	v_cvt_pk_f16_f32 v162, v236, v237
	v_cvt_pk_f16_f32 v163, v238, v239
	v_mfma_f32_16x16x32_f16 v[38:41], v[38:41], v[138:141], v[252:255]
	v_pk_max_f16 v162, v162, 0
	v_pk_max_f16 v163, v163, 0
	ds_write_b128 v108, v[160:163] offset:49152
	s_add_i32 s9, s22, s35
	s_waitcnt vmcnt(15)
	v_mfma_f32_16x16x32_f16 v[164:167], v[94:97], v[142:145], v[164:167]
	v_mfma_f32_16x16x32_f16 v[168:171], v[94:97], v[152:155], v[168:171]
	s_waitcnt vmcnt(14)
	v_mfma_f32_16x16x32_f16 v[58:61], v[90:93], v[142:145], v[58:61]
	v_mfma_f32_16x16x32_f16 v[176:179], v[90:93], v[152:155], v[176:179]
	s_waitcnt vmcnt(13)
	v_mfma_f32_16x16x32_f16 v[54:57], v[78:81], v[142:145], v[54:57]
	v_mfma_f32_16x16x32_f16 v[184:187], v[78:81], v[152:155], v[184:187]
	s_waitcnt vmcnt(12)
	v_mfma_f32_16x16x32_f16 v[50:53], v[34:37], v[142:145], v[50:53]
	buffer_load_dwordx4 v[140:143], v147, s[16:19], s9 offen
	buffer_load_dwordx4 v[220:223], v148, s[16:19], s9 offen
	v_mfma_f32_16x16x32_f16 v[122:125], v[34:37], v[152:155], v[122:125]
	buffer_load_dwordx4 v[152:155], v149, s[16:19], s9 offen
	buffer_load_dwordx4 v[224:227], v150, s[16:19], s9 offen
	s_mov_b32 s9, s21
	v_mfma_f32_16x16x32_f16 v[172:175], v[94:97], v[156:159], v[172:175]
	v_mfma_f32_16x16x32_f16 v[94:97], v[94:97], v[160:163], v[10:13]
	s_nop 2
	v_lshl_add_u64 v[10:11], s[8:9], 4, v[130:131]
	v_mfma_f32_16x16x32_f16 v[180:183], v[90:93], v[156:159], v[180:183]
	v_mfma_f32_16x16x32_f16 v[90:93], v[90:93], v[160:163], v[18:21]
	v_mfma_f32_16x16x32_f16 v[188:191], v[78:81], v[156:159], v[188:191]
	v_mfma_f32_16x16x32_f16 v[78:81], v[78:81], v[160:163], v[22:25]
	global_load_dwordx4 v[30:33], v[10:11], off
	s_nop 1
	global_load_dwordx4 v[22:25], v[10:11], off offset:1024
	global_load_dwordx4 v[18:21], v[10:11], off offset:2048
	s_nop 0
	global_load_dwordx4 v[10:13], v[10:11], off offset:3072
	s_nop 0
	global_load_dwordx2 v[134:135], v[0:1], off
	v_mfma_f32_16x16x32_f16 v[126:129], v[34:37], v[156:159], v[126:129]
	v_mfma_f32_16x16x32_f16 v[34:37], v[34:37], v[160:163], v[38:41]
	s_waitcnt lgkmcnt(0)
	s_barrier
	v_add_u32_e32 v99, s66, v99
	ds_read_b128 v[136:139], v99
	ds_read_b128 v[208:211], v99 offset:16384
	ds_read_b128 v[212:215], v99 offset:32768
	ds_read_b128 v[216:219], v99 offset:49152
	s_nop 2
	v_add_u32_e32 v100, s67, v100
	ds_read_b128 v[38:41], v100
	ds_read_b128 v[156:159], v100 offset:16384
	ds_read_b128 v[160:163], v100 offset:32768
	ds_read_b128 v[228:231], v100 offset:49152
	s_add_i32 s8, s22, s36
	s_waitcnt vmcnt(20) lgkmcnt(7)
	v_mfma_f32_16x16x32_f16 v[164:167], v[82:85], v[136:139], v[164:167]
	s_waitcnt lgkmcnt(6)
	v_mfma_f32_16x16x32_f16 v[168:171], v[82:85], v[208:211], v[168:171]
	s_waitcnt lgkmcnt(5)
	v_mfma_f32_16x16x32_f16 v[172:175], v[82:85], v[212:215], v[172:175]
	s_waitcnt lgkmcnt(4)
	v_mfma_f32_16x16x32_f16 v[82:85], v[82:85], v[216:219], v[94:97]
	s_waitcnt vmcnt(19)
	v_mfma_f32_16x16x32_f16 v[58:61], v[70:73], v[136:139], v[58:61]
	v_mfma_f32_16x16x32_f16 v[94:97], v[70:73], v[208:211], v[176:179]
	v_mfma_f32_16x16x32_f16 v[176:179], v[70:73], v[212:215], v[180:183]
	v_mfma_f32_16x16x32_f16 v[70:73], v[70:73], v[216:219], v[90:93]
	s_waitcnt vmcnt(18)
	v_mfma_f32_16x16x32_f16 v[54:57], v[62:65], v[136:139], v[54:57]
	v_mfma_f32_16x16x32_f16 v[90:93], v[62:65], v[208:211], v[184:187]
	v_mfma_f32_16x16x32_f16 v[180:183], v[62:65], v[212:215], v[188:191]
	v_mfma_f32_16x16x32_f16 v[62:65], v[62:65], v[216:219], v[78:81]
	s_waitcnt vmcnt(17)
	v_mfma_f32_16x16x32_f16 v[50:53], v[42:45], v[136:139], v[50:53]
	v_mfma_f32_16x16x32_f16 v[78:81], v[42:45], v[208:211], v[122:125]
	v_mfma_f32_16x16x32_f16 v[122:125], v[42:45], v[212:215], v[126:129]
	s_nop 2
	buffer_load_dwordx4 v[126:129], v147, s[16:19], s8 offen
	buffer_load_dwordx4 v[136:139], v148, s[16:19], s8 offen
	buffer_load_dwordx4 v[184:187], v149, s[16:19], s8 offen
	buffer_load_dwordx4 v[188:191], v150, s[16:19], s8 offen
	v_mfma_f32_16x16x32_f16 v[34:37], v[42:45], v[216:219], v[34:37]
	v_add_u32_e32 v111, s68, v111
	ds_read_b128 v[42:45], v111
	ds_read_b128 v[208:211], v111 offset:16384
	ds_read_b128 v[212:215], v111 offset:32768
	ds_read_b128 v[216:219], v111 offset:49152
	s_add_i32 s8, s22, s37
	s_waitcnt vmcnt(20) lgkmcnt(7)
	v_mfma_f32_16x16x32_f16 v[164:167], v[86:89], v[38:41], v[164:167]
	s_waitcnt lgkmcnt(6)
	v_mfma_f32_16x16x32_f16 v[168:171], v[86:89], v[156:159], v[168:171]
	s_waitcnt lgkmcnt(5)
	v_mfma_f32_16x16x32_f16 v[172:175], v[86:89], v[160:163], v[172:175]
	s_waitcnt lgkmcnt(4)
	v_mfma_f32_16x16x32_f16 v[82:85], v[86:89], v[228:231], v[82:85]
	s_waitcnt vmcnt(19)
	v_mfma_f32_16x16x32_f16 v[58:61], v[74:77], v[38:41], v[58:61]
	v_mfma_f32_16x16x32_f16 v[86:89], v[74:77], v[156:159], v[94:97]
	v_mfma_f32_16x16x32_f16 v[94:97], v[74:77], v[160:163], v[176:179]
	v_mfma_f32_16x16x32_f16 v[70:73], v[74:77], v[228:231], v[70:73]
	s_waitcnt vmcnt(18)
	v_mfma_f32_16x16x32_f16 v[54:57], v[66:69], v[38:41], v[54:57]
	v_mfma_f32_16x16x32_f16 v[74:77], v[66:69], v[156:159], v[90:93]
	v_mfma_f32_16x16x32_f16 v[90:93], v[66:69], v[160:163], v[180:183]
	v_mfma_f32_16x16x32_f16 v[62:65], v[66:69], v[228:231], v[62:65]
	s_waitcnt vmcnt(17)
	v_mfma_f32_16x16x32_f16 v[38:41], v[46:49], v[38:41], v[50:53]
	v_mfma_f32_16x16x32_f16 v[50:53], v[46:49], v[156:159], v[78:81]
	v_mfma_f32_16x16x32_f16 v[66:69], v[46:49], v[160:163], v[122:125]
	s_nop 1
	buffer_load_dwordx4 v[78:81], v147, s[16:19], s8 offen
	buffer_load_dwordx4 v[122:125], v148, s[16:19], s8 offen
	buffer_load_dwordx4 v[156:159], v149, s[16:19], s8 offen
	buffer_load_dwordx4 v[160:163], v150, s[16:19], s8 offen
	v_mfma_f32_16x16x32_f16 v[34:37], v[46:49], v[228:231], v[34:37]
	v_add_u32_e32 v98, s69, v98
	ds_read_b128 v[46:49], v98
	ds_read_b128 v[176:179], v98 offset:16384
	ds_read_b128 v[180:183], v98 offset:32768
	ds_read_b128 v[228:231], v98 offset:49152
	s_add_i32 s8, s22, s38
	s_waitcnt vmcnt(20) lgkmcnt(7)
	v_mfma_f32_16x16x32_f16 v[164:167], v[192:195], v[42:45], v[164:167]
	s_waitcnt lgkmcnt(6)
	v_mfma_f32_16x16x32_f16 v[168:171], v[192:195], v[208:211], v[168:171]
	s_waitcnt lgkmcnt(5)
	v_mfma_f32_16x16x32_f16 v[172:175], v[192:195], v[212:215], v[172:175]
	s_waitcnt lgkmcnt(4)
	v_mfma_f32_16x16x32_f16 v[82:85], v[192:195], v[216:219], v[82:85]
	s_waitcnt vmcnt(19)
	v_mfma_f32_16x16x32_f16 v[58:61], v[196:199], v[42:45], v[58:61]
	v_mfma_f32_16x16x32_f16 v[86:89], v[196:199], v[208:211], v[86:89]
	v_mfma_f32_16x16x32_f16 v[94:97], v[196:199], v[212:215], v[94:97]
	v_mfma_f32_16x16x32_f16 v[70:73], v[196:199], v[216:219], v[70:73]
	s_waitcnt vmcnt(18)
	v_mfma_f32_16x16x32_f16 v[54:57], v[200:203], v[42:45], v[54:57]
	v_mfma_f32_16x16x32_f16 v[74:77], v[200:203], v[208:211], v[74:77]
	v_mfma_f32_16x16x32_f16 v[90:93], v[200:203], v[212:215], v[90:93]
	v_mfma_f32_16x16x32_f16 v[62:65], v[200:203], v[216:219], v[62:65]
	s_waitcnt vmcnt(17)
	v_mfma_f32_16x16x32_f16 v[38:41], v[204:207], v[42:45], v[38:41]
	v_mfma_f32_16x16x32_f16 v[42:45], v[204:207], v[208:211], v[50:53]
	v_mfma_f32_16x16x32_f16 v[50:53], v[204:207], v[212:215], v[66:69]
	s_nop 2
	buffer_load_dwordx4 v[66:69], v147, s[16:19], s8 offen
	buffer_load_dwordx4 v[192:195], v148, s[16:19], s8 offen
	buffer_load_dwordx4 v[196:199], v149, s[16:19], s8 offen
	buffer_load_dwordx4 v[200:203], v150, s[16:19], s8 offen
	v_mfma_f32_16x16x32_f16 v[34:37], v[204:207], v[216:219], v[34:37]
	v_add_u32_e32 v99, s70, v99
	ds_read_b128 v[204:207], v99
	ds_read_b128 v[208:211], v99 offset:16384
	ds_read_b128 v[212:215], v99 offset:32768
	ds_read_b128 v[216:219], v99 offset:49152
	s_add_i32 s8, s22, s39
	s_waitcnt vmcnt(20) lgkmcnt(7)
	v_mfma_f32_16x16x32_f16 v[164:167], v[140:143], v[46:49], v[164:167]
	s_waitcnt lgkmcnt(6)
	v_mfma_f32_16x16x32_f16 v[168:171], v[140:143], v[176:179], v[168:171]
	s_waitcnt lgkmcnt(5)
	v_mfma_f32_16x16x32_f16 v[172:175], v[140:143], v[180:183], v[172:175]
	s_waitcnt lgkmcnt(4)
	v_mfma_f32_16x16x32_f16 v[82:85], v[140:143], v[228:231], v[82:85]
	s_waitcnt vmcnt(19)
	v_mfma_f32_16x16x32_f16 v[58:61], v[220:223], v[46:49], v[58:61]
	v_mfma_f32_16x16x32_f16 v[86:89], v[220:223], v[176:179], v[86:89]
	s_waitcnt vmcnt(18)
	v_mfma_f32_16x16x32_f16 v[54:57], v[152:155], v[46:49], v[54:57]
	v_mfma_f32_16x16x32_f16 v[74:77], v[152:155], v[176:179], v[74:77]
	v_mfma_f32_16x16x32_f16 v[90:93], v[152:155], v[180:183], v[90:93]
	v_mfma_f32_16x16x32_f16 v[62:65], v[152:155], v[228:231], v[62:65]
	s_waitcnt vmcnt(17)
	v_mfma_f32_16x16x32_f16 v[38:41], v[224:227], v[46:49], v[38:41]
	v_mfma_f32_16x16x32_f16 v[42:45], v[224:227], v[176:179], v[42:45]
	v_mfma_f32_16x16x32_f16 v[46:49], v[224:227], v[180:183], v[50:53]
	s_nop 2
	buffer_load_dwordx4 v[50:53], v147, s[16:19], s8 offen
	buffer_load_dwordx4 v[140:143], v148, s[16:19], s8 offen
	buffer_load_dwordx4 v[152:155], v149, s[16:19], s8 offen
	buffer_load_dwordx4 v[176:179], v150, s[16:19], s8 offen
	v_mfma_f32_16x16x32_f16 v[94:97], v[220:223], v[180:183], v[94:97]
	v_mfma_f32_16x16x32_f16 v[70:73], v[220:223], v[228:231], v[70:73]
	v_mfma_f32_16x16x32_f16 v[34:37], v[224:227], v[228:231], v[34:37]
	v_add_u32_e32 v100, s71, v100
	ds_read_b128 v[180:183], v100
	ds_read_b128 v[220:223], v100 offset:16384
	ds_read_b128 v[224:227], v100 offset:32768
	ds_read_b128 v[228:231], v100 offset:49152
	s_add_i32 s8, s22, s40
	s_waitcnt vmcnt(15) lgkmcnt(7)
	v_mfma_f32_16x16x32_f16 v[164:167], v[126:129], v[204:207], v[164:167]
	s_waitcnt lgkmcnt(6)
	v_mfma_f32_16x16x32_f16 v[168:171], v[126:129], v[208:211], v[168:171]
	s_waitcnt lgkmcnt(5)
	v_mfma_f32_16x16x32_f16 v[172:175], v[126:129], v[212:215], v[172:175]
	s_waitcnt lgkmcnt(4)
	v_mfma_f32_16x16x32_f16 v[82:85], v[126:129], v[216:219], v[82:85]
	s_waitcnt vmcnt(14)
	v_mfma_f32_16x16x32_f16 v[58:61], v[136:139], v[204:207], v[58:61]
	v_mfma_f32_16x16x32_f16 v[86:89], v[136:139], v[208:211], v[86:89]
	v_mfma_f32_16x16x32_f16 v[94:97], v[136:139], v[212:215], v[94:97]
	v_mfma_f32_16x16x32_f16 v[70:73], v[136:139], v[216:219], v[70:73]
	s_waitcnt vmcnt(13)
	v_mfma_f32_16x16x32_f16 v[54:57], v[184:187], v[204:207], v[54:57]
	v_mfma_f32_16x16x32_f16 v[74:77], v[184:187], v[208:211], v[74:77]
	v_mfma_f32_16x16x32_f16 v[90:93], v[184:187], v[212:215], v[90:93]
	v_mfma_f32_16x16x32_f16 v[62:65], v[184:187], v[216:219], v[62:65]
	s_waitcnt vmcnt(12)
	v_mfma_f32_16x16x32_f16 v[38:41], v[188:191], v[204:207], v[38:41]
	buffer_load_dwordx4 v[126:129], v147, s[16:19], s8 offen
	buffer_load_dwordx4 v[136:139], v148, s[16:19], s8 offen
	buffer_load_dwordx4 v[184:187], v149, s[16:19], s8 offen
	buffer_load_dwordx4 v[204:207], v150, s[16:19], s8 offen
	v_mfma_f32_16x16x32_f16 v[42:45], v[188:191], v[208:211], v[42:45]
	v_mfma_f32_16x16x32_f16 v[46:49], v[188:191], v[212:215], v[46:49]
	v_mfma_f32_16x16x32_f16 v[34:37], v[188:191], v[216:219], v[34:37]
	v_add_u32_e32 v111, s72, v111
	ds_read_b128 v[188:191], v111
	ds_read_b128 v[208:211], v111 offset:16384
	ds_read_b128 v[212:215], v111 offset:32768
	ds_read_b128 v[216:219], v111 offset:49152
	s_add_i32 s8, s22, s41
	s_waitcnt vmcnt(15) lgkmcnt(7)
	v_mfma_f32_16x16x32_f16 v[164:167], v[78:81], v[180:183], v[164:167]
	s_waitcnt lgkmcnt(6)
	v_mfma_f32_16x16x32_f16 v[168:171], v[78:81], v[220:223], v[168:171]
	s_waitcnt lgkmcnt(5)
	v_mfma_f32_16x16x32_f16 v[172:175], v[78:81], v[224:227], v[172:175]
	s_waitcnt lgkmcnt(4)
	v_mfma_f32_16x16x32_f16 v[78:81], v[78:81], v[228:231], v[82:85]
	s_waitcnt vmcnt(14)
	v_mfma_f32_16x16x32_f16 v[58:61], v[122:125], v[180:183], v[58:61]
	v_mfma_f32_16x16x32_f16 v[82:85], v[122:125], v[220:223], v[86:89]
	v_mfma_f32_16x16x32_f16 v[86:89], v[122:125], v[224:227], v[94:97]
	v_mfma_f32_16x16x32_f16 v[70:73], v[122:125], v[228:231], v[70:73]
	s_waitcnt vmcnt(13)
	v_mfma_f32_16x16x32_f16 v[54:57], v[156:159], v[180:183], v[54:57]
	v_mfma_f32_16x16x32_f16 v[74:77], v[156:159], v[220:223], v[74:77]
	v_mfma_f32_16x16x32_f16 v[90:93], v[156:159], v[224:227], v[90:93]
	v_mfma_f32_16x16x32_f16 v[62:65], v[156:159], v[228:231], v[62:65]
	s_waitcnt vmcnt(12)
	v_mfma_f32_16x16x32_f16 v[38:41], v[160:163], v[180:183], v[38:41]
	buffer_load_dwordx4 v[94:97], v147, s[16:19], s8 offen
	buffer_load_dwordx4 v[122:125], v148, s[16:19], s8 offen
	buffer_load_dwordx4 v[156:159], v149, s[16:19], s8 offen
	buffer_load_dwordx4 v[180:183], v150, s[16:19], s8 offen
	v_mfma_f32_16x16x32_f16 v[42:45], v[160:163], v[220:223], v[42:45]
	v_mfma_f32_16x16x32_f16 v[46:49], v[160:163], v[224:227], v[46:49]
	v_mfma_f32_16x16x32_f16 v[34:37], v[160:163], v[228:231], v[34:37]
	v_add_u32_e32 v98, s73, v98
	ds_read_b128 v[160:163], v98
	ds_read_b128 v[220:223], v98 offset:16384
	ds_read_b128 v[224:227], v98 offset:32768
	ds_read_b128 v[228:231], v98 offset:49152
	s_add_i32 s8, s22, s42
	s_waitcnt vmcnt(15) lgkmcnt(7)
	v_mfma_f32_16x16x32_f16 v[164:167], v[66:69], v[188:191], v[164:167]
	s_waitcnt lgkmcnt(6)
	v_mfma_f32_16x16x32_f16 v[168:171], v[66:69], v[208:211], v[168:171]
	s_waitcnt lgkmcnt(5)
	v_mfma_f32_16x16x32_f16 v[172:175], v[66:69], v[212:215], v[172:175]
	s_waitcnt lgkmcnt(4)
	v_mfma_f32_16x16x32_f16 v[66:69], v[66:69], v[216:219], v[78:81]
	s_waitcnt vmcnt(14)
	v_mfma_f32_16x16x32_f16 v[58:61], v[192:195], v[188:191], v[58:61]
	v_mfma_f32_16x16x32_f16 v[78:81], v[192:195], v[208:211], v[82:85]
	v_mfma_f32_16x16x32_f16 v[82:85], v[192:195], v[212:215], v[86:89]
	v_mfma_f32_16x16x32_f16 v[70:73], v[192:195], v[216:219], v[70:73]
	s_waitcnt vmcnt(13)
	v_mfma_f32_16x16x32_f16 v[54:57], v[196:199], v[188:191], v[54:57]
	v_mfma_f32_16x16x32_f16 v[74:77], v[196:199], v[208:211], v[74:77]
	v_mfma_f32_16x16x32_f16 v[86:89], v[196:199], v[212:215], v[90:93]
	v_mfma_f32_16x16x32_f16 v[62:65], v[196:199], v[216:219], v[62:65]
	s_waitcnt vmcnt(12)
	v_mfma_f32_16x16x32_f16 v[38:41], v[200:203], v[188:191], v[38:41]
	buffer_load_dwordx4 v[90:93], v147, s[16:19], s8 offen
	buffer_load_dwordx4 v[188:191], v148, s[16:19], s8 offen
	buffer_load_dwordx4 v[192:195], v149, s[16:19], s8 offen
	buffer_load_dwordx4 v[196:199], v150, s[16:19], s8 offen
	v_mfma_f32_16x16x32_f16 v[42:45], v[200:203], v[208:211], v[42:45]
	v_mfma_f32_16x16x32_f16 v[46:49], v[200:203], v[212:215], v[46:49]
	v_mfma_f32_16x16x32_f16 v[34:37], v[200:203], v[216:219], v[34:37]
	v_add_u32_e32 v99, s74, v99
	ds_read_b128 v[200:203], v99
	ds_read_b128 v[208:211], v99 offset:16384
	ds_read_b128 v[212:215], v99 offset:32768
	ds_read_b128 v[216:219], v99 offset:49152
	s_add_i32 s8, s22, s43
	s_waitcnt vmcnt(15) lgkmcnt(7)
	v_mfma_f32_16x16x32_f16 v[164:167], v[50:53], v[160:163], v[164:167]
	s_waitcnt lgkmcnt(6)
	v_mfma_f32_16x16x32_f16 v[168:171], v[50:53], v[220:223], v[168:171]
	s_waitcnt lgkmcnt(5)
	v_mfma_f32_16x16x32_f16 v[172:175], v[50:53], v[224:227], v[172:175]
	s_waitcnt lgkmcnt(4)
	v_mfma_f32_16x16x32_f16 v[50:53], v[50:53], v[228:231], v[66:69]
	s_waitcnt vmcnt(14)
	v_mfma_f32_16x16x32_f16 v[58:61], v[140:143], v[160:163], v[58:61]
	v_mfma_f32_16x16x32_f16 v[66:69], v[140:143], v[220:223], v[78:81]
	v_mfma_f32_16x16x32_f16 v[78:81], v[140:143], v[224:227], v[82:85]
	v_mfma_f32_16x16x32_f16 v[70:73], v[140:143], v[228:231], v[70:73]
	s_waitcnt vmcnt(13)
	v_mfma_f32_16x16x32_f16 v[54:57], v[152:155], v[160:163], v[54:57]
	v_mfma_f32_16x16x32_f16 v[74:77], v[152:155], v[220:223], v[74:77]
	v_mfma_f32_16x16x32_f16 v[82:85], v[152:155], v[224:227], v[86:89]
	v_mfma_f32_16x16x32_f16 v[62:65], v[152:155], v[228:231], v[62:65]
	s_waitcnt vmcnt(12)
	v_mfma_f32_16x16x32_f16 v[38:41], v[176:179], v[160:163], v[38:41]
	buffer_load_dwordx4 v[86:89], v147, s[16:19], s8 offen
	buffer_load_dwordx4 v[140:143], v148, s[16:19], s8 offen
	buffer_load_dwordx4 v[152:155], v149, s[16:19], s8 offen
	buffer_load_dwordx4 v[160:163], v150, s[16:19], s8 offen
	v_mfma_f32_16x16x32_f16 v[42:45], v[176:179], v[220:223], v[42:45]
	v_mfma_f32_16x16x32_f16 v[46:49], v[176:179], v[224:227], v[46:49]
	v_mfma_f32_16x16x32_f16 v[34:37], v[176:179], v[228:231], v[34:37]
	v_add_u32_e32 v100, s75, v100
	ds_read_b128 v[176:179], v100
	ds_read_b128 v[220:223], v100 offset:16384
	ds_read_b128 v[224:227], v100 offset:32768
	ds_read_b128 v[228:231], v100 offset:49152
	s_add_i32 s8, s22, s44
	s_waitcnt vmcnt(15) lgkmcnt(7)
	v_mfma_f32_16x16x32_f16 v[164:167], v[126:129], v[200:203], v[164:167]
	s_waitcnt lgkmcnt(6)
	v_mfma_f32_16x16x32_f16 v[168:171], v[126:129], v[208:211], v[168:171]
	s_waitcnt lgkmcnt(5)
	v_mfma_f32_16x16x32_f16 v[172:175], v[126:129], v[212:215], v[172:175]
	s_waitcnt lgkmcnt(4)
	v_mfma_f32_16x16x32_f16 v[50:53], v[126:129], v[216:219], v[50:53]
	s_waitcnt vmcnt(14)
	v_mfma_f32_16x16x32_f16 v[58:61], v[136:139], v[200:203], v[58:61]
	v_mfma_f32_16x16x32_f16 v[66:69], v[136:139], v[208:211], v[66:69]
	v_mfma_f32_16x16x32_f16 v[78:81], v[136:139], v[212:215], v[78:81]
	v_mfma_f32_16x16x32_f16 v[70:73], v[136:139], v[216:219], v[70:73]
	s_waitcnt vmcnt(13)
	v_mfma_f32_16x16x32_f16 v[54:57], v[184:187], v[200:203], v[54:57]
	v_mfma_f32_16x16x32_f16 v[74:77], v[184:187], v[208:211], v[74:77]
	v_mfma_f32_16x16x32_f16 v[82:85], v[184:187], v[212:215], v[82:85]
	v_mfma_f32_16x16x32_f16 v[62:65], v[184:187], v[216:219], v[62:65]
	s_waitcnt vmcnt(12)
	v_mfma_f32_16x16x32_f16 v[38:41], v[204:207], v[200:203], v[38:41]
	buffer_load_dwordx4 v[126:129], v147, s[16:19], s8 offen
	buffer_load_dwordx4 v[136:139], v148, s[16:19], s8 offen
	buffer_load_dwordx4 v[184:187], v149, s[16:19], s8 offen
	buffer_load_dwordx4 v[200:203], v150, s[16:19], s8 offen
	v_mfma_f32_16x16x32_f16 v[42:45], v[204:207], v[208:211], v[42:45]
	v_mfma_f32_16x16x32_f16 v[46:49], v[204:207], v[212:215], v[46:49]
	v_mfma_f32_16x16x32_f16 v[34:37], v[204:207], v[216:219], v[34:37]
	v_add_u32_e32 v111, s76, v111
	ds_read_b128 v[204:207], v111
	ds_read_b128 v[208:211], v111 offset:16384
	ds_read_b128 v[212:215], v111 offset:32768
	ds_read_b128 v[216:219], v111 offset:49152
	s_add_i32 s8, s22, s45
	s_waitcnt vmcnt(15) lgkmcnt(7)
	v_mfma_f32_16x16x32_f16 v[164:167], v[94:97], v[176:179], v[164:167]
	s_waitcnt lgkmcnt(6)
	v_mfma_f32_16x16x32_f16 v[168:171], v[94:97], v[220:223], v[168:171]
	s_waitcnt vmcnt(14)
	v_mfma_f32_16x16x32_f16 v[58:61], v[122:125], v[176:179], v[58:61]
	v_mfma_f32_16x16x32_f16 v[66:69], v[122:125], v[220:223], v[66:69]
	s_waitcnt lgkmcnt(5)
	v_mfma_f32_16x16x32_f16 v[78:81], v[122:125], v[224:227], v[78:81]
	s_waitcnt lgkmcnt(4)
	v_mfma_f32_16x16x32_f16 v[70:73], v[122:125], v[228:231], v[70:73]
	s_waitcnt vmcnt(13)
	v_mfma_f32_16x16x32_f16 v[54:57], v[156:159], v[176:179], v[54:57]
	v_mfma_f32_16x16x32_f16 v[74:77], v[156:159], v[220:223], v[74:77]
	v_mfma_f32_16x16x32_f16 v[82:85], v[156:159], v[224:227], v[82:85]
	v_mfma_f32_16x16x32_f16 v[62:65], v[156:159], v[228:231], v[62:65]
	s_waitcnt vmcnt(12)
	v_mfma_f32_16x16x32_f16 v[38:41], v[180:183], v[176:179], v[38:41]
	v_mfma_f32_16x16x32_f16 v[42:45], v[180:183], v[220:223], v[42:45]
	buffer_load_dwordx4 v[122:125], v147, s[16:19], s8 offen
	buffer_load_dwordx4 v[156:159], v148, s[16:19], s8 offen
	buffer_load_dwordx4 v[176:179], v149, s[16:19], s8 offen
	buffer_load_dwordx4 v[220:223], v150, s[16:19], s8 offen
	v_mfma_f32_16x16x32_f16 v[50:53], v[94:97], v[228:231], v[50:53]
	v_mfma_f32_16x16x32_f16 v[46:49], v[180:183], v[224:227], v[46:49]
	v_mfma_f32_16x16x32_f16 v[34:37], v[180:183], v[228:231], v[34:37]
	v_mfma_f32_16x16x32_f16 v[172:175], v[94:97], v[224:227], v[172:175]
	v_add_u32_e32 v98, s77, v98
	ds_read_b128 v[94:97], v98
	ds_read_b128 v[180:183], v98 offset:16384
	ds_read_b128 v[224:227], v98 offset:32768
	ds_read_b128 v[228:231], v98 offset:49152
	s_add_i32 s8, s22, s46
	s_waitcnt vmcnt(15) lgkmcnt(7)
	v_mfma_f32_16x16x32_f16 v[164:167], v[90:93], v[204:207], v[164:167]
	s_waitcnt lgkmcnt(6)
	v_mfma_f32_16x16x32_f16 v[168:171], v[90:93], v[208:211], v[168:171]
	s_waitcnt lgkmcnt(5)
	v_mfma_f32_16x16x32_f16 v[172:175], v[90:93], v[212:215], v[172:175]
	s_waitcnt lgkmcnt(4)
	v_mfma_f32_16x16x32_f16 v[90:93], v[90:93], v[216:219], v[50:53]
	s_waitcnt vmcnt(14)
	v_mfma_f32_16x16x32_f16 v[232:235], v[188:191], v[204:207], v[58:61]
	v_mfma_f32_16x16x32_f16 v[66:69], v[188:191], v[208:211], v[66:69]
	v_mfma_f32_16x16x32_f16 v[78:81], v[188:191], v[212:215], v[78:81]
	v_mfma_f32_16x16x32_f16 v[70:73], v[188:191], v[216:219], v[70:73]
	s_waitcnt vmcnt(13)
	v_mfma_f32_16x16x32_f16 v[188:191], v[192:195], v[204:207], v[54:57]
	v_mfma_f32_16x16x32_f16 v[74:77], v[192:195], v[208:211], v[74:77]
	v_mfma_f32_16x16x32_f16 v[82:85], v[192:195], v[212:215], v[82:85]
	v_mfma_f32_16x16x32_f16 v[62:65], v[192:195], v[216:219], v[62:65]
	s_waitcnt vmcnt(12)
	v_mfma_f32_16x16x32_f16 v[192:195], v[196:199], v[204:207], v[38:41]
	buffer_load_dwordx4 v[58:61], v147, s[16:19], s8 offen
	buffer_load_dwordx4 v[54:57], v148, s[16:19], s8 offen
	buffer_load_dwordx4 v[50:53], v149, s[16:19], s8 offen
	buffer_load_dwordx4 v[38:41], v150, s[16:19], s8 offen
	v_mfma_f32_16x16x32_f16 v[42:45], v[196:199], v[208:211], v[42:45]
	v_mfma_f32_16x16x32_f16 v[46:49], v[196:199], v[212:215], v[46:49]
	v_mfma_f32_16x16x32_f16 v[196:199], v[196:199], v[216:219], v[34:37]
	v_add_u32_e32 v99, s78, v99
	ds_read_b128 v[204:207], v99
	ds_read_b128 v[208:211], v99 offset:16384
	ds_read_b128 v[212:215], v99 offset:32768
	ds_read_b128 v[216:219], v99 offset:49152
	s_add_i32 s8, s22, s47
	s_waitcnt vmcnt(15) lgkmcnt(7)
	v_mfma_f32_16x16x32_f16 v[164:167], v[86:89], v[94:97], v[164:167]
	s_waitcnt lgkmcnt(6)
	v_mfma_f32_16x16x32_f16 v[168:171], v[86:89], v[180:183], v[168:171]
	s_waitcnt lgkmcnt(5)
	v_mfma_f32_16x16x32_f16 v[172:175], v[86:89], v[224:227], v[172:175]
	s_waitcnt lgkmcnt(4)
	v_mfma_f32_16x16x32_f16 v[86:89], v[86:89], v[228:231], v[90:93]
	s_waitcnt vmcnt(14)
	v_mfma_f32_16x16x32_f16 v[232:235], v[140:143], v[94:97], v[232:235]
	v_mfma_f32_16x16x32_f16 v[66:69], v[140:143], v[180:183], v[66:69]
	v_mfma_f32_16x16x32_f16 v[236:239], v[140:143], v[224:227], v[78:81]
	v_mfma_f32_16x16x32_f16 v[70:73], v[140:143], v[228:231], v[70:73]
	s_waitcnt vmcnt(13)
	v_mfma_f32_16x16x32_f16 v[140:143], v[152:155], v[94:97], v[188:191]
	v_mfma_f32_16x16x32_f16 v[74:77], v[152:155], v[180:183], v[74:77]
	v_mfma_f32_16x16x32_f16 v[82:85], v[152:155], v[224:227], v[82:85]
	v_mfma_f32_16x16x32_f16 v[62:65], v[152:155], v[228:231], v[62:65]
	s_waitcnt vmcnt(12)
	v_mfma_f32_16x16x32_f16 v[152:155], v[160:163], v[94:97], v[192:195]
	buffer_load_dwordx4 v[94:97], v147, s[16:19], s8 offen
	buffer_load_dwordx4 v[90:93], v148, s[16:19], s8 offen
	buffer_load_dwordx4 v[78:81], v149, s[16:19], s8 offen
	buffer_load_dwordx4 v[34:37], v150, s[16:19], s8 offen
	v_mfma_f32_16x16x32_f16 v[42:45], v[160:163], v[180:183], v[42:45]
	v_mfma_f32_16x16x32_f16 v[46:49], v[160:163], v[224:227], v[46:49]
	v_mfma_f32_16x16x32_f16 v[160:163], v[160:163], v[228:231], v[196:199]
	v_add_u32_e32 v100, s79, v100
	ds_read_b128 v[180:183], v100
	ds_read_b128 v[188:191], v100 offset:16384
	ds_read_b128 v[192:195], v100 offset:32768
	ds_read_b128 v[196:199], v100 offset:49152
	s_add_i32 s8, s22, s48
	s_waitcnt vmcnt(15) lgkmcnt(7)
	v_mfma_f32_16x16x32_f16 v[164:167], v[126:129], v[204:207], v[164:167]
	s_waitcnt lgkmcnt(6)
	v_mfma_f32_16x16x32_f16 v[168:171], v[126:129], v[208:211], v[168:171]
	s_waitcnt lgkmcnt(5)
	v_mfma_f32_16x16x32_f16 v[172:175], v[126:129], v[212:215], v[172:175]
	s_waitcnt lgkmcnt(4)
	v_mfma_f32_16x16x32_f16 v[86:89], v[126:129], v[216:219], v[86:89]
	s_waitcnt vmcnt(14)
	v_mfma_f32_16x16x32_f16 v[126:129], v[136:139], v[204:207], v[232:235]
	v_mfma_f32_16x16x32_f16 v[66:69], v[136:139], v[208:211], v[66:69]
	v_mfma_f32_16x16x32_f16 v[224:227], v[136:139], v[212:215], v[236:239]
	v_mfma_f32_16x16x32_f16 v[136:139], v[136:139], v[216:219], v[70:73]
	s_waitcnt vmcnt(13)
	v_mfma_f32_16x16x32_f16 v[140:143], v[184:187], v[204:207], v[140:143]
	v_mfma_f32_16x16x32_f16 v[74:77], v[184:187], v[208:211], v[74:77]
	v_mfma_f32_16x16x32_f16 v[228:231], v[184:187], v[212:215], v[82:85]
	v_mfma_f32_16x16x32_f16 v[184:187], v[184:187], v[216:219], v[62:65]
	s_waitcnt vmcnt(12)
	v_mfma_f32_16x16x32_f16 v[152:155], v[200:203], v[204:207], v[152:155]
	v_mfma_f32_16x16x32_f16 v[204:207], v[200:203], v[208:211], v[42:45]
	buffer_load_dwordx4 v[82:85], v147, s[16:19], s8 offen
	buffer_load_dwordx4 v[70:73], v148, s[16:19], s8 offen
	buffer_load_dwordx4 v[62:65], v149, s[16:19], s8 offen
	buffer_load_dwordx4 v[42:45], v150, s[16:19], s8 offen
	v_mfma_f32_16x16x32_f16 v[46:49], v[200:203], v[212:215], v[46:49]
	v_mfma_f32_16x16x32_f16 v[160:163], v[200:203], v[216:219], v[160:163]
	v_add_u32_e32 v0, 0x1ac00, v104
	ds_read_b128 v[240:243], v0
	ds_read_b128 v[244:247], v0 offset:16
	s_waitcnt vmcnt(12) lgkmcnt(5)
	v_mfma_f32_16x16x32_f16 v[164:167], v[122:125], v[180:183], v[164:167]
	v_mfma_f32_16x16x32_f16 v[126:129], v[156:159], v[180:183], v[126:129]
	v_mfma_f32_16x16x32_f16 v[140:143], v[176:179], v[180:183], v[140:143]
	v_mfma_f32_16x16x32_f16 v[152:155], v[220:223], v[180:183], v[152:155]
	s_waitcnt lgkmcnt(4)
	v_mfma_f32_16x16x32_f16 v[168:171], v[122:125], v[188:191], v[168:171]
	v_mfma_f32_16x16x32_f16 v[208:211], v[156:159], v[188:191], v[66:69]
	v_mfma_f32_16x16x32_f16 v[212:215], v[176:179], v[188:191], v[74:77]
	v_mfma_f32_16x16x32_f16 v[204:207], v[220:223], v[188:191], v[204:207]
	s_waitcnt lgkmcnt(3)
	v_mfma_f32_16x16x32_f16 v[172:175], v[122:125], v[192:195], v[172:175]
	v_cvt_pk_f16_f32 v232, v164, v165
	v_cvt_pk_f16_f32 v233, v166, v167
	v_pk_max_f16 v232, v232, 0
	v_pk_max_f16 v233, v233, 0
	v_mfma_f32_16x16x32_f16 v[224:227], v[156:159], v[192:195], v[224:227]
	v_cvt_pk_f16_f32 v234, v126, v127
	v_cvt_pk_f16_f32 v235, v128, v129
	v_pk_max_f16 v234, v234, 0
	v_pk_max_f16 v235, v235, 0
	v_mfma_f32_16x16x32_f16 v[228:231], v[176:179], v[192:195], v[228:231]
	v_cvt_pk_f16_f32 v236, v140, v141
	v_cvt_pk_f16_f32 v237, v142, v143
	v_pk_max_f16 v236, v236, 0
	v_pk_max_f16 v237, v237, 0
	v_mfma_f32_16x16x32_f16 v[216:219], v[220:223], v[192:195], v[46:49]
	v_cvt_pk_f16_f32 v238, v152, v153
	v_cvt_pk_f16_f32 v239, v154, v155
	v_pk_max_f16 v238, v238, 0
	v_pk_max_f16 v239, v239, 0
	s_waitcnt lgkmcnt(2)
	v_mfma_f32_16x16x32_f16 v[200:203], v[122:125], v[196:199], v[86:89]
	v_cvt_pk_f16_f32 v180, v168, v169
	v_cvt_pk_f16_f32 v181, v170, v171
	v_pk_max_f16 v180, v180, 0
	v_pk_max_f16 v181, v181, 0
	s_add_i32 s8, s22, s49
	buffer_load_dwordx4 v[86:89], v147, s[16:19], s8 offen
	buffer_load_dwordx4 v[74:77], v148, s[16:19], s8 offen
	buffer_load_dwordx4 v[66:69], v149, s[16:19], s8 offen
	buffer_load_dwordx4 v[46:49], v150, s[16:19], s8 offen
	v_mfma_f32_16x16x32_f16 v[136:139], v[156:159], v[196:199], v[136:139]
	v_cvt_pk_f16_f32 v182, v208, v209
	v_cvt_pk_f16_f32 v183, v210, v211
	v_pk_max_f16 v182, v182, 0
	v_pk_max_f16 v183, v183, 0
	s_waitcnt lgkmcnt(1)
	v_mfma_f32_16x16x32_f16 v[252:255], v[240:243], v[232:235], 0
	v_cvt_pk_f16_f32 v232, v172, v173
	v_cvt_pk_f16_f32 v233, v174, v175
	v_pk_max_f16 v232, v232, 0
	v_pk_max_f16 v233, v233, 0
	v_mfma_f32_16x16x32_f16 v[184:187], v[176:179], v[196:199], v[184:187]
	v_cvt_pk_f16_f32 v188, v212, v213
	v_cvt_pk_f16_f32 v189, v214, v215
	v_pk_max_f16 v188, v188, 0
	v_pk_max_f16 v189, v189, 0
	s_waitcnt lgkmcnt(0)
	v_mfma_f32_16x16x32_f16 v[252:255], v[244:247], v[236:239], v[252:255]
	ds_read_u16 v102, v114
	ds_read_u16 v103, v114 offset:512
	ds_read_u16 v115, v114 offset:1024
	ds_read_u16 v116, v114 offset:1536
	v_cvt_pk_f16_f32 v234, v224, v225
	v_cvt_pk_f16_f32 v235, v226, v227
	v_pk_max_f16 v234, v234, 0
	v_pk_max_f16 v235, v235, 0
	v_mfma_f32_16x16x32_f16 v[160:163], v[220:223], v[196:199], v[160:163]
	v_cvt_pk_f16_f32 v190, v204, v205
	v_cvt_pk_f16_f32 v191, v206, v207
	v_pk_max_f16 v190, v190, 0
	v_pk_max_f16 v191, v191, 0
	v_mfma_f32_16x16x32_f16 v[192:195], v[240:243], v[180:183], 0
	v_cvt_pk_f16_f32 v236, v228, v229
	v_cvt_pk_f16_f32 v237, v230, v231
	v_pk_max_f16 v236, v236, 0
	v_pk_max_f16 v237, v237, 0
	v_mfma_f32_16x16x32_f16 v[192:195], v[244:247], v[188:191], v[192:195]
	v_cvt_pk_f16_f32 v238, v216, v217
	v_cvt_pk_f16_f32 v239, v218, v219
	v_pk_max_f16 v238, v238, 0
	v_pk_max_f16 v239, v239, 0
	v_cvt_pk_f16_f32 v180, v200, v201
	v_cvt_pk_f16_f32 v181, v202, v203
	v_pk_max_f16 v180, v180, 0
	v_pk_max_f16 v181, v181, 0
	v_mfma_f32_16x16x32_f16 v[196:199], v[240:243], v[232:235], 0
	v_cvt_pk_f16_f32 v182, v136, v137
	v_cvt_pk_f16_f32 v183, v138, v139
	v_pk_max_f16 v182, v182, 0
	v_pk_max_f16 v183, v183, 0
	v_mfma_f32_16x16x32_f16 v[196:199], v[244:247], v[236:239], v[196:199]
	v_cvt_pk_f16_f32 v188, v184, v185
	v_cvt_pk_f16_f32 v189, v186, v187
	v_pk_max_f16 v188, v188, 0
	v_pk_max_f16 v189, v189, 0
	v_cvt_pk_f16_f32 v190, v160, v161
	v_cvt_pk_f16_f32 v191, v162, v163
	v_pk_max_f16 v190, v190, 0
	v_pk_max_f16 v191, v191, 0
	v_mfma_f32_16x16x32_f16 v[122:125], v[240:243], v[180:183], 0
	s_nop 0
	v_mfma_f32_16x16x32_f16 v[122:125], v[244:247], v[188:191], v[122:125]
	v_add_u32_e32 v145, 0x12c00, v105
	ds_read_b128 v[240:243], v145 offset:2048
	ds_read_b128 v[244:247], v145 offset:2064
	ds_read_b128 v[248:251], v145 offset:2080
	s_load_dword s30, s[12:13], 0x0
	v_cndmask_b32_e64 v0, v252, v192, s[2:3]
	ds_read_b128 v[252:255], v145 offset:2096
	v_cndmask_b32_e64 v0, v0, v196, s[0:1]
	v_cndmask_b32_e64 v0, v0, v122, s[26:27]
	ds_write_b32 v112, v0
	s_waitcnt vmcnt(16)
	v_cndmask_b32_e64 v1, v30, v134, s[0:1]
	v_bfi_b32 v30, s10, v1, v30
	v_perm_b32 v1, v22, v134, s24
	v_cndmask_b32_e64 v22, v22, v1, s[0:1]
	v_bfi_b32 v1, s10, v135, v18
	v_perm_b32 v121, v10, v135, s24
	v_cndmask_b32_e64 v18, v18, v1, s[0:1]
	v_cndmask_b32_e64 v10, v10, v121, s[0:1]
	s_add_i32 s22, s22, 0x80000
	s_add_i32 s11, s11, 1
	s_add_u32 s12, s12, 4
	s_addc_u32 s13, s13, 0
	v_add_u32_e32 v104, 0x400, v104
	v_add_u32_e32 v105, 0x800, v105
	v_add_u32_e32 v114, 2, v114
	s_cmp_eq_u32 s22, 0x898000
	s_waitcnt lgkmcnt(0)
	s_barrier
	ds_read_b128 v[232:235], v113
	ds_read_b128 v[236:239], v113 offset:1024
	s_waitcnt lgkmcnt(0)
	v_add_f32_e32 v0, v232, v233
	v_add_f32_e32 v1, v234, v235
	v_add_f32_e32 v121, v236, v237
	v_add_f32_e32 v144, v238, v239
	v_add_f32_e32 v0, v0, v1
	v_add_f32_e32 v121, v121, v144
	v_add_f32_e32 v0, v0, v121
	v_add_f32_e32 v0, s30, v0
	ds_write_b32 v106, v0
	v_cvt_f16_f32_e32 v1, v0
	v_cvt_f16_f32_e32 v121, v0
	s_nop 1
	v_permlane16_swap_b32_e32 v1, v121
	v_mov_b32_e32 v144, v1
	v_mov_b32_e32 v145, v121
	s_nop 1
	v_permlane32_swap_b32_e32 v1, v144
	v_permlane32_swap_b32_e32 v121, v145
	v_add_u32_e32 v106, 4, v106
	s_cbranch_scc0 .LBB1_4
